# baseline (speedup 1.0000x reference)
_Z11center_mainPKfPKcS0_Pf:
	s_load_dwordx4 s[4:7], s[0:1], 0x0
	s_load_dwordx4 s[8:11], s[0:1], 0x10
	s_and_b32 s3, s2, 7
	s_lshr_b32 s12, s2, 3
	s_mov_b32 s30, s2
	v_lshrrev_b32_e32 v1, 6, v0
	v_and_b32_e32 v2, 63, v0
	v_bfe_u32 v3, v0, 3, 3
	v_and_b32_e32 v4, 7, v0
	v_lshrrev_b32_e32 v5, 7, v0
	v_bfe_u32 v6, v0, 6, 1
	v_lshl_or_b32 v7, v5, 3, v3
	v_lshlrev_b32_e32 v8, 10, v7
	v_lshl_or_b32 v8, v6, 9, v8
	v_lshl_or_b32 v226, v4, 4, v8
	v_lshlrev_b32_e32 v17, 15, v1
	v_lshl_or_b32 v227, v2, 5, v17
	v_lshlrev_b32_e32 v237, 3, v0
	s_lshl_b32 s13, s3, 22
	s_lshl_b32 s14, s12, 15
	s_add_u32 s13, s13, s14
	s_lshl_b32 s15, s3, 18
	s_lshl_b32 s28, s3, 12
	s_waitcnt lgkmcnt(0)
	s_add_u32 s16, s4, s13
	s_addc_u32 s17, s5, 0
	global_load_dwordx4 v[194:197], v226, s[16:17] offset:0 nt
	global_load_dwordx4 v[198:201], v226, s[16:17] offset:128 nt
	global_load_dwordx4 v[202:205], v226, s[16:17] offset:256 nt
	global_load_dwordx4 v[206:209], v226, s[16:17] offset:384 nt
	s_add_u32 s8, s8, s28
	s_addc_u32 s9, s9, 0
	global_load_dwordx2 v[238:239], v237, s[8:9]
	s_add_u32 s24, s6, s15
	s_addc_u32 s25, s7, 0
	s_add_u32 s32, s24, 0x1000
	s_addc_u32 s33, s25, 0
	s_add_u32 s34, s24, 0x2000
	s_addc_u32 s35, s25, 0
	s_add_u32 s36, s24, 0x3000
	s_addc_u32 s37, s25, 0
	s_add_u32 s38, s24, 0x4000
	s_addc_u32 s39, s25, 0
	s_add_u32 s40, s24, 0x5000
	s_addc_u32 s41, s25, 0
	s_add_u32 s42, s24, 0x6000
	s_addc_u32 s43, s25, 0
	s_add_u32 s44, s24, 0x7000
	s_addc_u32 s45, s25, 0
	global_load_dwordx4 v[34:37], v227, s[24:25] offset:0
	global_load_dwordx4 v[38:41], v227, s[24:25] offset:16
	global_load_dwordx4 v[26:29], v227, s[24:25] offset:2048
	global_load_dwordx4 v[30:33], v227, s[24:25] offset:2064
	global_load_dwordx4 v[50:53], v227, s[32:33] offset:0
	global_load_dwordx4 v[54:57], v227, s[32:33] offset:16
	global_load_dwordx4 v[42:45], v227, s[32:33] offset:2048
	global_load_dwordx4 v[46:49], v227, s[32:33] offset:2064
	global_load_dwordx4 v[18:21], v227, s[34:35] offset:0
	global_load_dwordx4 v[22:25], v227, s[34:35] offset:16
	global_load_dwordx4 v[130:133], v227, s[34:35] offset:2048
	global_load_dwordx4 v[134:137], v227, s[34:35] offset:2064
	global_load_dwordx4 v[122:125], v227, s[36:37] offset:0
	global_load_dwordx4 v[126:129], v227, s[36:37] offset:16
	global_load_dwordx4 v[138:141], v227, s[36:37] offset:2048
	global_load_dwordx4 v[142:145], v227, s[36:37] offset:2064
	global_load_dwordx4 v[98:101], v227, s[38:39] offset:0
	global_load_dwordx4 v[102:105], v227, s[38:39] offset:16
	global_load_dwordx4 v[90:93], v227, s[38:39] offset:2048
	global_load_dwordx4 v[94:97], v227, s[38:39] offset:2064
	global_load_dwordx4 v[114:117], v227, s[40:41] offset:0
	global_load_dwordx4 v[118:121], v227, s[40:41] offset:16
	global_load_dwordx4 v[106:109], v227, s[40:41] offset:2048
	global_load_dwordx4 v[110:113], v227, s[40:41] offset:2064
	global_load_dwordx4 v[58:61], v227, s[42:43] offset:0
	global_load_dwordx4 v[62:65], v227, s[42:43] offset:16
	global_load_dwordx4 v[66:69], v227, s[42:43] offset:2048
	global_load_dwordx4 v[70:73], v227, s[42:43] offset:2064
	global_load_dwordx4 v[74:77], v227, s[44:45] offset:0
	global_load_dwordx4 v[78:81], v227, s[44:45] offset:16
	global_load_dwordx4 v[82:85], v227, s[44:45] offset:2048
	global_load_dwordx4 v[86:89], v227, s[44:45] offset:2064
	s_add_u32 s18, s16, 0x100000
	s_addc_u32 s19, s17, 0
	s_add_u32 s20, s16, 0x200000
	s_addc_u32 s21, s17, 0
	s_add_u32 s22, s16, 0x300000
	s_addc_u32 s23, s17, 0
	v_mul_u32_u24_e32 v9, 0x110, v7
	v_lshl_add_u32 v9, v6, 7, v9
	v_lshl_add_u32 v228, v4, 4, v9
	v_lshlrev_b32_e32 v10, 6, v7
	v_lshl_or_b32 v10, v6, 5, v10
	v_lshl_or_b32 v229, v4, 2, v10
	v_and_b32_e32 v11, 31, v0
	v_bfe_u32 v12, v0, 5, 1
	v_mul_u32_u24_e32 v13, 0x110, v11
	v_lshl_add_u32 v230, v12, 5, v13
	v_lshlrev_b32_e32 v14, 9, v1
	v_lshl_or_b32 v231, v12, 4, v14
	v_xor_b32_e32 v15, 32, v2
	v_lshlrev_b32_e32 v232, 2, v15
	v_xor_b32_e32 v15, 16, v2
	v_lshlrev_b32_e32 v247, 2, v15
	v_lshlrev_b32_e32 v16, 7, v1
	v_lshl_or_b32 v233, v11, 2, v16
	v_mov_b32_e32 v234, 0x7f7f7f7f
	s_waitcnt vmcnt(32)
	ds_write_b64 v237, v[238:239] offset:34816
	v_mul_f32_e32 v244, v194, v194
	v_mul_f32_e32 v245, v198, v198
	v_cvt_pk_fp8_f32 v240, v194, v195
	v_cvt_pk_fp8_f32 v241, v198, v199
	v_cvt_pk_fp8_f32 v242, v202, v203
	v_cvt_pk_fp8_f32 v243, v206, v207
	v_fmac_f32_e32 v244, v195, v195
	v_fmac_f32_e32 v245, v199, v199
	v_fmac_f32_e32 v244, v196, v196
	v_fmac_f32_e32 v245, v200, v200
	v_fmac_f32_e32 v244, v197, v197
	v_fmac_f32_e32 v245, v201, v201
	v_fmac_f32_e32 v244, v202, v202
	v_fmac_f32_e32 v245, v206, v206
	v_fmac_f32_e32 v244, v203, v203
	v_fmac_f32_e32 v245, v207, v207
	v_fmac_f32_e32 v244, v204, v204
	v_fmac_f32_e32 v245, v208, v208
	v_fmac_f32_e32 v244, v205, v205
	v_fmac_f32_e32 v245, v209, v209
	v_cvt_pk_fp8_f32 v240, v196, v197 op_sel:[0,0,1]
	v_cvt_pk_fp8_f32 v241, v200, v201 op_sel:[0,0,1]
	v_cvt_pk_fp8_f32 v242, v204, v205 op_sel:[0,0,1]
	v_cvt_pk_fp8_f32 v243, v208, v209 op_sel:[0,0,1]
	v_add_f32_e32 v244, v244, v245
	s_nop 0
	ds_write_b128 v228, v[240:243] offset:0
	ds_write_b32 v229, v244 offset:38912
	global_load_dwordx4 v[210:213], v226, s[18:19] offset:0 nt
	global_load_dwordx4 v[214:217], v226, s[18:19] offset:128 nt
	global_load_dwordx4 v[218:221], v226, s[18:19] offset:256 nt
	global_load_dwordx4 v[222:225], v226, s[18:19] offset:384 nt
	s_waitcnt lgkmcnt(0)
	s_barrier
	ds_read_b128 v[162:165], v230 offset:0
	ds_read_b128 v[166:169], v230 offset:16
	ds_read_b128 v[2:5], v231 offset:34816
	ds_read_b128 v[6:9], v231 offset:34848
	ds_read_b128 v[10:13], v231 offset:34880
	ds_read_b128 v[14:17], v231 offset:34912
	ds_read_b128 v[170:173], v230 offset:64
	ds_read_b128 v[174:177], v230 offset:80
	ds_read_b128 v[178:181], v230 offset:128
	ds_read_b128 v[182:185], v230 offset:144
	ds_read_b128 v[186:189], v230 offset:192
	ds_read_b128 v[190:193], v230 offset:208
	s_waitcnt vmcnt(34) lgkmcnt(6)
	v_mfma_scale_f32_32x32x64_f8f6f4 v[2:17], v[34:41], v[162:169], v[2:17], v234, v234 op_sel_hi:[0,0,0]
	s_waitcnt vmcnt(32) lgkmcnt(4)
	v_mfma_scale_f32_32x32x64_f8f6f4 v[2:17], v[26:33], v[170:177], v[2:17], v234, v234 op_sel_hi:[0,0,0]
	ds_read_b128 v[146:149], v231 offset:34944
	ds_read_b128 v[150:153], v231 offset:34976
	ds_read_b128 v[154:157], v231 offset:35008
	ds_read_b128 v[158:161], v231 offset:35040
	s_waitcnt vmcnt(30) lgkmcnt(6)
	v_mfma_scale_f32_32x32x64_f8f6f4 v[2:17], v[50:57], v[178:185], v[2:17], v234, v234 op_sel_hi:[0,0,0]
	s_waitcnt vmcnt(28) lgkmcnt(4)
	v_mfma_scale_f32_32x32x64_f8f6f4 v[2:17], v[42:49], v[186:193], v[2:17], v234, v234 op_sel_hi:[0,0,0]
	s_waitcnt lgkmcnt(0)
	s_waitcnt vmcnt(26)
	v_mfma_scale_f32_32x32x64_f8f6f4 v[146:161], v[18:25], v[162:169], v[146:161], v234, v234 op_sel_hi:[0,0,0]
	s_waitcnt vmcnt(24)
	v_mfma_scale_f32_32x32x64_f8f6f4 v[146:161], v[130:137], v[170:177], v[146:161], v234, v234 op_sel_hi:[0,0,0]
	v_min3_f32 v2, v2, v3, v4
	v_min3_f32 v5, v5, v6, v7
	v_min3_f32 v8, v8, v9, v10
	v_min3_f32 v11, v11, v12, v13
	v_min3_f32 v14, v14, v15, v16
	v_min3_f32 v2, v2, v5, v8
	v_min3_f32 v11, v11, v14, v17
	v_min_f32_e32 v235, v2, v11
	ds_read_b128 v[2:5], v231 offset:35072
	ds_read_b128 v[6:9], v231 offset:35104
	ds_read_b128 v[10:13], v231 offset:35136
	ds_read_b128 v[14:17], v231 offset:35168
	s_waitcnt vmcnt(22)
	v_mfma_scale_f32_32x32x64_f8f6f4 v[146:161], v[122:129], v[178:185], v[146:161], v234, v234 op_sel_hi:[0,0,0]
	s_waitcnt vmcnt(20)
	v_mfma_scale_f32_32x32x64_f8f6f4 v[146:161], v[138:145], v[186:193], v[146:161], v234, v234 op_sel_hi:[0,0,0]
	s_waitcnt vmcnt(18) lgkmcnt(0)
	v_mfma_scale_f32_32x32x64_f8f6f4 v[2:17], v[98:105], v[162:169], v[2:17], v234, v234 op_sel_hi:[0,0,0]
	s_waitcnt vmcnt(16)
	v_mfma_scale_f32_32x32x64_f8f6f4 v[2:17], v[90:97], v[170:177], v[2:17], v234, v234 op_sel_hi:[0,0,0]
	v_min3_f32 v146, v146, v147, v148
	v_min3_f32 v149, v149, v150, v151
	v_min3_f32 v152, v152, v153, v154
	v_min3_f32 v155, v155, v156, v157
	v_min3_f32 v158, v158, v159, v160
	v_min3_f32 v146, v146, v149, v152
	v_min3_f32 v155, v155, v158, v161
	v_min3_f32 v235, v235, v146, v155
	ds_read_b128 v[146:149], v231 offset:35200
	ds_read_b128 v[150:153], v231 offset:35232
	ds_read_b128 v[154:157], v231 offset:35264
	ds_read_b128 v[158:161], v231 offset:35296
	s_waitcnt vmcnt(14)
	v_mfma_scale_f32_32x32x64_f8f6f4 v[2:17], v[114:121], v[178:185], v[2:17], v234, v234 op_sel_hi:[0,0,0]
	s_waitcnt vmcnt(12)
	v_mfma_scale_f32_32x32x64_f8f6f4 v[2:17], v[106:113], v[186:193], v[2:17], v234, v234 op_sel_hi:[0,0,0]
	s_waitcnt vmcnt(10) lgkmcnt(0)
	v_mfma_scale_f32_32x32x64_f8f6f4 v[146:161], v[58:65], v[162:169], v[146:161], v234, v234 op_sel_hi:[0,0,0]
	s_waitcnt vmcnt(8)
	v_mfma_scale_f32_32x32x64_f8f6f4 v[146:161], v[66:73], v[170:177], v[146:161], v234, v234 op_sel_hi:[0,0,0]
	v_min3_f32 v2, v2, v3, v4
	v_min3_f32 v5, v5, v6, v7
	v_min3_f32 v8, v8, v9, v10
	v_min3_f32 v11, v11, v12, v13
	v_min3_f32 v14, v14, v15, v16
	v_min3_f32 v2, v2, v5, v8
	v_min3_f32 v11, v11, v14, v17
	v_min3_f32 v235, v235, v2, v11
	ds_read_b128 v[2:5], v231 offset:34816
	ds_read_b128 v[6:9], v231 offset:34848
	ds_read_b128 v[10:13], v231 offset:34880
	ds_read_b128 v[14:17], v231 offset:34912
	s_waitcnt vmcnt(6)
	v_mfma_scale_f32_32x32x64_f8f6f4 v[146:161], v[74:81], v[178:185], v[146:161], v234, v234 op_sel_hi:[0,0,0]
	s_waitcnt vmcnt(4)
	v_mfma_scale_f32_32x32x64_f8f6f4 v[146:161], v[82:89], v[186:193], v[146:161], v234, v234 op_sel_hi:[0,0,0]
	global_load_dwordx4 v[194:197], v226, s[20:21] offset:0 nt
	global_load_dwordx4 v[198:201], v226, s[20:21] offset:128 nt
	global_load_dwordx4 v[202:205], v226, s[20:21] offset:256 nt
	global_load_dwordx4 v[206:209], v226, s[20:21] offset:384 nt
	s_waitcnt vmcnt(4)
	v_mul_f32_e32 v244, v210, v210
	v_mul_f32_e32 v245, v214, v214
	v_cvt_pk_fp8_f32 v240, v210, v211
	v_cvt_pk_fp8_f32 v241, v214, v215
	v_cvt_pk_fp8_f32 v242, v218, v219
	v_cvt_pk_fp8_f32 v243, v222, v223
	v_fmac_f32_e32 v244, v211, v211
	v_fmac_f32_e32 v245, v215, v215
	v_fmac_f32_e32 v244, v212, v212
	v_fmac_f32_e32 v245, v216, v216
	v_fmac_f32_e32 v244, v213, v213
	v_fmac_f32_e32 v245, v217, v217
	v_fmac_f32_e32 v244, v218, v218
	v_fmac_f32_e32 v245, v222, v222
	v_fmac_f32_e32 v244, v219, v219
	v_fmac_f32_e32 v245, v223, v223
	v_fmac_f32_e32 v244, v220, v220
	v_fmac_f32_e32 v245, v224, v224
	v_fmac_f32_e32 v244, v221, v221
	v_fmac_f32_e32 v245, v225, v225
	v_cvt_pk_fp8_f32 v240, v212, v213 op_sel:[0,0,1]
	v_cvt_pk_fp8_f32 v241, v216, v217 op_sel:[0,0,1]
	v_cvt_pk_fp8_f32 v242, v220, v221 op_sel:[0,0,1]
	v_cvt_pk_fp8_f32 v243, v224, v225 op_sel:[0,0,1]
	v_add_f32_e32 v244, v244, v245
	s_nop 0
	ds_write_b128 v228, v[240:243] offset:8704
	ds_write_b32 v229, v244 offset:40960
	s_waitcnt lgkmcnt(0)
	s_barrier
	ds_read_b128 v[162:165], v230 offset:8704
	ds_read_b128 v[166:169], v230 offset:8720
	ds_read_b128 v[170:173], v230 offset:8768
	ds_read_b128 v[174:177], v230 offset:8784
	ds_read_b128 v[178:181], v230 offset:8832
	ds_read_b128 v[182:185], v230 offset:8848
	ds_read_b128 v[186:189], v230 offset:8896
	ds_read_b128 v[190:193], v230 offset:8912
	s_waitcnt lgkmcnt(6)
	v_mfma_scale_f32_32x32x64_f8f6f4 v[2:17], v[34:41], v[162:169], v[2:17], v234, v234 op_sel_hi:[0,0,0]
	s_waitcnt lgkmcnt(4)
	v_mfma_scale_f32_32x32x64_f8f6f4 v[2:17], v[26:33], v[170:177], v[2:17], v234, v234 op_sel_hi:[0,0,0]
	v_min3_f32 v146, v146, v147, v148
	v_min3_f32 v149, v149, v150, v151
	v_min3_f32 v152, v152, v153, v154
	v_min3_f32 v155, v155, v156, v157
	v_min3_f32 v158, v158, v159, v160
	v_min3_f32 v146, v146, v149, v152
	v_min3_f32 v155, v155, v158, v161
	v_min3_f32 v235, v235, v146, v155
	ds_bpermute_b32 v246, v232, v235
	ds_read_b128 v[146:149], v231 offset:34944
	ds_read_b128 v[150:153], v231 offset:34976
	ds_read_b128 v[154:157], v231 offset:35008
	ds_read_b128 v[158:161], v231 offset:35040
	s_waitcnt lgkmcnt(7)
	v_mfma_scale_f32_32x32x64_f8f6f4 v[2:17], v[50:57], v[178:185], v[2:17], v234, v234 op_sel_hi:[0,0,0]
	s_waitcnt lgkmcnt(5)
	v_mfma_scale_f32_32x32x64_f8f6f4 v[2:17], v[42:49], v[186:193], v[2:17], v234, v234 op_sel_hi:[0,0,0]
	s_waitcnt lgkmcnt(0)
	v_min_f32_e32 v246, v235, v246
	ds_write_b32 v233, v246 offset:47104
	v_mfma_scale_f32_32x32x64_f8f6f4 v[146:161], v[18:25], v[162:169], v[146:161], v234, v234 op_sel_hi:[0,0,0]
	v_mfma_scale_f32_32x32x64_f8f6f4 v[146:161], v[130:137], v[170:177], v[146:161], v234, v234 op_sel_hi:[0,0,0]
	v_min3_f32 v2, v2, v3, v4
	v_min3_f32 v5, v5, v6, v7
	v_min3_f32 v8, v8, v9, v10
	v_min3_f32 v11, v11, v12, v13
	v_min3_f32 v14, v14, v15, v16
	v_min3_f32 v2, v2, v5, v8
	v_min3_f32 v11, v11, v14, v17
	v_min_f32_e32 v236, v2, v11
	ds_read_b128 v[2:5], v231 offset:35072
	ds_read_b128 v[6:9], v231 offset:35104
	ds_read_b128 v[10:13], v231 offset:35136
	ds_read_b128 v[14:17], v231 offset:35168
	v_mfma_scale_f32_32x32x64_f8f6f4 v[146:161], v[122:129], v[178:185], v[146:161], v234, v234 op_sel_hi:[0,0,0]
	v_mfma_scale_f32_32x32x64_f8f6f4 v[146:161], v[138:145], v[186:193], v[146:161], v234, v234 op_sel_hi:[0,0,0]
	s_waitcnt lgkmcnt(0)
	v_mfma_scale_f32_32x32x64_f8f6f4 v[2:17], v[98:105], v[162:169], v[2:17], v234, v234 op_sel_hi:[0,0,0]
	v_mfma_scale_f32_32x32x64_f8f6f4 v[2:17], v[90:97], v[170:177], v[2:17], v234, v234 op_sel_hi:[0,0,0]
	v_min3_f32 v146, v146, v147, v148
	v_min3_f32 v149, v149, v150, v151
	v_min3_f32 v152, v152, v153, v154
	v_min3_f32 v155, v155, v156, v157
	v_min3_f32 v158, v158, v159, v160
	v_min3_f32 v146, v146, v149, v152
	v_min3_f32 v155, v155, v158, v161
	v_min3_f32 v236, v236, v146, v155
	ds_read_b128 v[146:149], v231 offset:35200
	ds_read_b128 v[150:153], v231 offset:35232
	ds_read_b128 v[154:157], v231 offset:35264
	ds_read_b128 v[158:161], v231 offset:35296
	v_mfma_scale_f32_32x32x64_f8f6f4 v[2:17], v[114:121], v[178:185], v[2:17], v234, v234 op_sel_hi:[0,0,0]
	v_mfma_scale_f32_32x32x64_f8f6f4 v[2:17], v[106:113], v[186:193], v[2:17], v234, v234 op_sel_hi:[0,0,0]
	s_waitcnt lgkmcnt(0)
	v_mfma_scale_f32_32x32x64_f8f6f4 v[146:161], v[58:65], v[162:169], v[146:161], v234, v234 op_sel_hi:[0,0,0]
	v_mfma_scale_f32_32x32x64_f8f6f4 v[146:161], v[66:73], v[170:177], v[146:161], v234, v234 op_sel_hi:[0,0,0]
	v_min3_f32 v2, v2, v3, v4
	v_min3_f32 v5, v5, v6, v7
	v_min3_f32 v8, v8, v9, v10
	v_min3_f32 v11, v11, v12, v13
	v_min3_f32 v14, v14, v15, v16
	v_min3_f32 v2, v2, v5, v8
	v_min3_f32 v11, v11, v14, v17
	v_min3_f32 v236, v236, v2, v11
	ds_read_b128 v[2:5], v231 offset:34816
	ds_read_b128 v[6:9], v231 offset:34848
	ds_read_b128 v[10:13], v231 offset:34880
	ds_read_b128 v[14:17], v231 offset:34912
	v_mfma_scale_f32_32x32x64_f8f6f4 v[146:161], v[74:81], v[178:185], v[146:161], v234, v234 op_sel_hi:[0,0,0]
	v_mfma_scale_f32_32x32x64_f8f6f4 v[146:161], v[82:89], v[186:193], v[146:161], v234, v234 op_sel_hi:[0,0,0]
	global_load_dwordx4 v[210:213], v226, s[22:23] offset:0 nt
	global_load_dwordx4 v[214:217], v226, s[22:23] offset:128 nt
	global_load_dwordx4 v[218:221], v226, s[22:23] offset:256 nt
	global_load_dwordx4 v[222:225], v226, s[22:23] offset:384 nt
	s_waitcnt vmcnt(4)
	v_mul_f32_e32 v244, v194, v194
	v_mul_f32_e32 v245, v198, v198
	v_cvt_pk_fp8_f32 v240, v194, v195
	v_cvt_pk_fp8_f32 v241, v198, v199
	v_cvt_pk_fp8_f32 v242, v202, v203
	v_cvt_pk_fp8_f32 v243, v206, v207
	v_fmac_f32_e32 v244, v195, v195
	v_fmac_f32_e32 v245, v199, v199
	v_fmac_f32_e32 v244, v196, v196
	v_fmac_f32_e32 v245, v200, v200
	v_fmac_f32_e32 v244, v197, v197
	v_fmac_f32_e32 v245, v201, v201
	v_fmac_f32_e32 v244, v202, v202
	v_fmac_f32_e32 v245, v206, v206
	v_fmac_f32_e32 v244, v203, v203
	v_fmac_f32_e32 v245, v207, v207
	v_fmac_f32_e32 v244, v204, v204
	v_fmac_f32_e32 v245, v208, v208
	v_fmac_f32_e32 v244, v205, v205
	v_fmac_f32_e32 v245, v209, v209
	v_cvt_pk_fp8_f32 v240, v196, v197 op_sel:[0,0,1]
	v_cvt_pk_fp8_f32 v241, v200, v201 op_sel:[0,0,1]
	v_cvt_pk_fp8_f32 v242, v204, v205 op_sel:[0,0,1]
	v_cvt_pk_fp8_f32 v243, v208, v209 op_sel:[0,0,1]
	v_add_f32_e32 v244, v244, v245
	s_nop 0
	ds_write_b128 v228, v[240:243] offset:17408
	ds_write_b32 v229, v244 offset:43008
	s_waitcnt lgkmcnt(0)
	s_barrier
	ds_read_b128 v[162:165], v230 offset:17408
	ds_read_b128 v[166:169], v230 offset:17424
	ds_read_b128 v[170:173], v230 offset:17472
	ds_read_b128 v[174:177], v230 offset:17488
	ds_read_b128 v[178:181], v230 offset:17536
	ds_read_b128 v[182:185], v230 offset:17552
	ds_read_b128 v[186:189], v230 offset:17600
	ds_read_b128 v[190:193], v230 offset:17616
	s_waitcnt lgkmcnt(6)
	v_mfma_scale_f32_32x32x64_f8f6f4 v[2:17], v[34:41], v[162:169], v[2:17], v234, v234 op_sel_hi:[0,0,0]
	s_waitcnt lgkmcnt(4)
	v_mfma_scale_f32_32x32x64_f8f6f4 v[2:17], v[26:33], v[170:177], v[2:17], v234, v234 op_sel_hi:[0,0,0]
	v_min3_f32 v146, v146, v147, v148
	v_min3_f32 v149, v149, v150, v151
	v_min3_f32 v152, v152, v153, v154
	v_min3_f32 v155, v155, v156, v157
	v_min3_f32 v158, v158, v159, v160
	v_min3_f32 v146, v146, v149, v152
	v_min3_f32 v155, v155, v158, v161
	v_min3_f32 v236, v236, v146, v155
	ds_bpermute_b32 v246, v232, v236
	ds_read_b128 v[146:149], v231 offset:34944
	ds_read_b128 v[150:153], v231 offset:34976
	ds_read_b128 v[154:157], v231 offset:35008
	ds_read_b128 v[158:161], v231 offset:35040
	s_waitcnt lgkmcnt(7)
	v_mfma_scale_f32_32x32x64_f8f6f4 v[2:17], v[50:57], v[178:185], v[2:17], v234, v234 op_sel_hi:[0,0,0]
	s_waitcnt lgkmcnt(5)
	v_mfma_scale_f32_32x32x64_f8f6f4 v[2:17], v[42:49], v[186:193], v[2:17], v234, v234 op_sel_hi:[0,0,0]
	s_waitcnt lgkmcnt(0)
	v_min_f32_e32 v246, v236, v246
	ds_write_b32 v233, v246 offset:48128
	v_mfma_scale_f32_32x32x64_f8f6f4 v[146:161], v[18:25], v[162:169], v[146:161], v234, v234 op_sel_hi:[0,0,0]
	v_mfma_scale_f32_32x32x64_f8f6f4 v[146:161], v[130:137], v[170:177], v[146:161], v234, v234 op_sel_hi:[0,0,0]
	v_min3_f32 v2, v2, v3, v4
	v_min3_f32 v5, v5, v6, v7
	v_min3_f32 v8, v8, v9, v10
	v_min3_f32 v11, v11, v12, v13
	v_min3_f32 v14, v14, v15, v16
	v_min3_f32 v2, v2, v5, v8
	v_min3_f32 v11, v11, v14, v17
	v_min_f32_e32 v235, v2, v11
	ds_read_b128 v[2:5], v231 offset:35072
	ds_read_b128 v[6:9], v231 offset:35104
	ds_read_b128 v[10:13], v231 offset:35136
	ds_read_b128 v[14:17], v231 offset:35168
	v_mfma_scale_f32_32x32x64_f8f6f4 v[146:161], v[122:129], v[178:185], v[146:161], v234, v234 op_sel_hi:[0,0,0]
	v_mfma_scale_f32_32x32x64_f8f6f4 v[146:161], v[138:145], v[186:193], v[146:161], v234, v234 op_sel_hi:[0,0,0]
	s_waitcnt lgkmcnt(0)
	v_mfma_scale_f32_32x32x64_f8f6f4 v[2:17], v[98:105], v[162:169], v[2:17], v234, v234 op_sel_hi:[0,0,0]
	v_mfma_scale_f32_32x32x64_f8f6f4 v[2:17], v[90:97], v[170:177], v[2:17], v234, v234 op_sel_hi:[0,0,0]
	v_min3_f32 v146, v146, v147, v148
	v_min3_f32 v149, v149, v150, v151
	v_min3_f32 v152, v152, v153, v154
	v_min3_f32 v155, v155, v156, v157
	v_min3_f32 v158, v158, v159, v160
	v_min3_f32 v146, v146, v149, v152
	v_min3_f32 v155, v155, v158, v161
	v_min3_f32 v235, v235, v146, v155
	ds_read_b128 v[146:149], v231 offset:35200
	ds_read_b128 v[150:153], v231 offset:35232
	ds_read_b128 v[154:157], v231 offset:35264
	ds_read_b128 v[158:161], v231 offset:35296
	v_mfma_scale_f32_32x32x64_f8f6f4 v[2:17], v[114:121], v[178:185], v[2:17], v234, v234 op_sel_hi:[0,0,0]
	v_mfma_scale_f32_32x32x64_f8f6f4 v[2:17], v[106:113], v[186:193], v[2:17], v234, v234 op_sel_hi:[0,0,0]
	s_waitcnt lgkmcnt(0)
	v_mfma_scale_f32_32x32x64_f8f6f4 v[146:161], v[58:65], v[162:169], v[146:161], v234, v234 op_sel_hi:[0,0,0]
	v_mfma_scale_f32_32x32x64_f8f6f4 v[146:161], v[66:73], v[170:177], v[146:161], v234, v234 op_sel_hi:[0,0,0]
	v_min3_f32 v2, v2, v3, v4
	v_min3_f32 v5, v5, v6, v7
	v_min3_f32 v8, v8, v9, v10
	v_min3_f32 v11, v11, v12, v13
	v_min3_f32 v14, v14, v15, v16
	v_min3_f32 v2, v2, v5, v8
	v_min3_f32 v11, v11, v14, v17
	v_min3_f32 v235, v235, v2, v11
	ds_read_b128 v[2:5], v231 offset:34816
	ds_read_b128 v[6:9], v231 offset:34848
	ds_read_b128 v[10:13], v231 offset:34880
	ds_read_b128 v[14:17], v231 offset:34912
	v_mfma_scale_f32_32x32x64_f8f6f4 v[146:161], v[74:81], v[178:185], v[146:161], v234, v234 op_sel_hi:[0,0,0]
	v_mfma_scale_f32_32x32x64_f8f6f4 v[146:161], v[82:89], v[186:193], v[146:161], v234, v234 op_sel_hi:[0,0,0]
	s_waitcnt vmcnt(0)
	v_mul_f32_e32 v244, v210, v210
	v_mul_f32_e32 v245, v214, v214
	v_cvt_pk_fp8_f32 v240, v210, v211
	v_cvt_pk_fp8_f32 v241, v214, v215
	v_cvt_pk_fp8_f32 v242, v218, v219
	v_cvt_pk_fp8_f32 v243, v222, v223
	v_fmac_f32_e32 v244, v211, v211
	v_fmac_f32_e32 v245, v215, v215
	v_fmac_f32_e32 v244, v212, v212
	v_fmac_f32_e32 v245, v216, v216
	v_fmac_f32_e32 v244, v213, v213
	v_fmac_f32_e32 v245, v217, v217
	v_fmac_f32_e32 v244, v218, v218
	v_fmac_f32_e32 v245, v222, v222
	v_fmac_f32_e32 v244, v219, v219
	v_fmac_f32_e32 v245, v223, v223
	v_fmac_f32_e32 v244, v220, v220
	v_fmac_f32_e32 v245, v224, v224
	v_fmac_f32_e32 v244, v221, v221
	v_fmac_f32_e32 v245, v225, v225
	v_cvt_pk_fp8_f32 v240, v212, v213 op_sel:[0,0,1]
	v_cvt_pk_fp8_f32 v241, v216, v217 op_sel:[0,0,1]
	v_cvt_pk_fp8_f32 v242, v220, v221 op_sel:[0,0,1]
	v_cvt_pk_fp8_f32 v243, v224, v225 op_sel:[0,0,1]
	v_add_f32_e32 v244, v244, v245
	s_nop 0
	ds_write_b128 v228, v[240:243] offset:26112
	ds_write_b32 v229, v244 offset:45056
	s_waitcnt lgkmcnt(0)
	s_barrier
	ds_read_b128 v[162:165], v230 offset:26112
	ds_read_b128 v[166:169], v230 offset:26128
	ds_read_b128 v[170:173], v230 offset:26176
	ds_read_b128 v[174:177], v230 offset:26192
	ds_read_b128 v[178:181], v230 offset:26240
	ds_read_b128 v[182:185], v230 offset:26256
	ds_read_b128 v[186:189], v230 offset:26304
	ds_read_b128 v[190:193], v230 offset:26320
	s_waitcnt lgkmcnt(6)
	v_mfma_scale_f32_32x32x64_f8f6f4 v[2:17], v[34:41], v[162:169], v[2:17], v234, v234 op_sel_hi:[0,0,0]
	s_waitcnt lgkmcnt(4)
	v_mfma_scale_f32_32x32x64_f8f6f4 v[2:17], v[26:33], v[170:177], v[2:17], v234, v234 op_sel_hi:[0,0,0]
	v_min3_f32 v146, v146, v147, v148
	v_min3_f32 v149, v149, v150, v151
	v_min3_f32 v152, v152, v153, v154
	v_min3_f32 v155, v155, v156, v157
	v_min3_f32 v158, v158, v159, v160
	v_min3_f32 v146, v146, v149, v152
	v_min3_f32 v155, v155, v158, v161
	v_min3_f32 v235, v235, v146, v155
	ds_bpermute_b32 v246, v232, v235
	ds_read_b128 v[146:149], v231 offset:34944
	ds_read_b128 v[150:153], v231 offset:34976
	ds_read_b128 v[154:157], v231 offset:35008
	ds_read_b128 v[158:161], v231 offset:35040
	s_waitcnt lgkmcnt(7)
	v_mfma_scale_f32_32x32x64_f8f6f4 v[2:17], v[50:57], v[178:185], v[2:17], v234, v234 op_sel_hi:[0,0,0]
	s_waitcnt lgkmcnt(5)
	v_mfma_scale_f32_32x32x64_f8f6f4 v[2:17], v[42:49], v[186:193], v[2:17], v234, v234 op_sel_hi:[0,0,0]
	s_waitcnt lgkmcnt(0)
	v_min_f32_e32 v246, v235, v246
	ds_write_b32 v233, v246 offset:49152
	v_mfma_scale_f32_32x32x64_f8f6f4 v[146:161], v[18:25], v[162:169], v[146:161], v234, v234 op_sel_hi:[0,0,0]
	v_mfma_scale_f32_32x32x64_f8f6f4 v[146:161], v[130:137], v[170:177], v[146:161], v234, v234 op_sel_hi:[0,0,0]
	v_min3_f32 v2, v2, v3, v4
	v_min3_f32 v5, v5, v6, v7
	v_min3_f32 v8, v8, v9, v10
	v_min3_f32 v11, v11, v12, v13
	v_min3_f32 v14, v14, v15, v16
	v_min3_f32 v2, v2, v5, v8
	v_min3_f32 v11, v11, v14, v17
	v_min_f32_e32 v236, v2, v11
	ds_read_b128 v[2:5], v231 offset:35072
	ds_read_b128 v[6:9], v231 offset:35104
	ds_read_b128 v[10:13], v231 offset:35136
	ds_read_b128 v[14:17], v231 offset:35168
	v_mfma_scale_f32_32x32x64_f8f6f4 v[146:161], v[122:129], v[178:185], v[146:161], v234, v234 op_sel_hi:[0,0,0]
	v_mfma_scale_f32_32x32x64_f8f6f4 v[146:161], v[138:145], v[186:193], v[146:161], v234, v234 op_sel_hi:[0,0,0]
	s_waitcnt lgkmcnt(0)
	v_mfma_scale_f32_32x32x64_f8f6f4 v[2:17], v[98:105], v[162:169], v[2:17], v234, v234 op_sel_hi:[0,0,0]
	v_mfma_scale_f32_32x32x64_f8f6f4 v[2:17], v[90:97], v[170:177], v[2:17], v234, v234 op_sel_hi:[0,0,0]
	v_min3_f32 v146, v146, v147, v148
	v_min3_f32 v149, v149, v150, v151
	v_min3_f32 v152, v152, v153, v154
	v_min3_f32 v155, v155, v156, v157
	v_min3_f32 v158, v158, v159, v160
	v_min3_f32 v146, v146, v149, v152
	v_min3_f32 v155, v155, v158, v161
	v_min3_f32 v236, v236, v146, v155
	ds_read_b128 v[146:149], v231 offset:35200
	ds_read_b128 v[150:153], v231 offset:35232
	ds_read_b128 v[154:157], v231 offset:35264
	ds_read_b128 v[158:161], v231 offset:35296
	v_mfma_scale_f32_32x32x64_f8f6f4 v[2:17], v[114:121], v[178:185], v[2:17], v234, v234 op_sel_hi:[0,0,0]
	v_mfma_scale_f32_32x32x64_f8f6f4 v[2:17], v[106:113], v[186:193], v[2:17], v234, v234 op_sel_hi:[0,0,0]
	s_waitcnt lgkmcnt(0)
	v_mfma_scale_f32_32x32x64_f8f6f4 v[146:161], v[58:65], v[162:169], v[146:161], v234, v234 op_sel_hi:[0,0,0]
	v_mfma_scale_f32_32x32x64_f8f6f4 v[146:161], v[66:73], v[170:177], v[146:161], v234, v234 op_sel_hi:[0,0,0]
	v_min3_f32 v2, v2, v3, v4
	v_min3_f32 v5, v5, v6, v7
	v_min3_f32 v8, v8, v9, v10
	v_min3_f32 v11, v11, v12, v13
	v_min3_f32 v14, v14, v15, v16
	v_min3_f32 v2, v2, v5, v8
	v_min3_f32 v11, v11, v14, v17
	v_min3_f32 v236, v236, v2, v11
	v_mfma_scale_f32_32x32x64_f8f6f4 v[146:161], v[74:81], v[178:185], v[146:161], v234, v234 op_sel_hi:[0,0,0]
	v_mfma_scale_f32_32x32x64_f8f6f4 v[146:161], v[82:89], v[186:193], v[146:161], v234, v234 op_sel_hi:[0,0,0]
	v_cmp_gt_u32_e32 vcc, 0x80, v0
	s_and_saveexec_b64 s[34:35], vcc
	v_lshlrev_b32_e32 v36, 6, v0
	ds_read_b128 v[20:23], v36 offset:38912
	ds_read_b128 v[24:27], v36 offset:38928
	ds_read_b128 v[28:31], v36 offset:38944
	ds_read_b128 v[32:35], v36 offset:38960
	s_mov_b64 exec, s[34:35]
	s_nop 15
	s_nop 3
	v_min3_f32 v146, v146, v147, v148
	v_min3_f32 v149, v149, v150, v151
	v_min3_f32 v152, v152, v153, v154
	v_min3_f32 v155, v155, v156, v157
	v_min3_f32 v158, v158, v159, v160
	v_min3_f32 v146, v146, v149, v152
	v_min3_f32 v155, v155, v158, v161
	v_min3_f32 v236, v236, v146, v155
	ds_bpermute_b32 v246, v232, v236
	s_waitcnt lgkmcnt(0)
	v_min_f32_e32 v246, v236, v246
	ds_write_b32 v233, v246 offset:50176
	s_waitcnt lgkmcnt(0)
	s_barrier
	v_readfirstlane_b32 s2, v1
	s_nop 3
	s_cmp_gt_u32 s2, 1
	s_cbranch_scc1 .Lmain_end
	v_and_b32_e32 v2, 31, v0
	v_lshlrev_b32_e32 v3, 5, v0
	v_and_b32_e32 v3, 0xc00, v3
	v_lshl_or_b32 v8, v2, 2, v3
	v_add_u32_e32 v8, 0xb800, v8
	ds_read2_b32 v[2:3], v8 offset1:32
	ds_read2_b32 v[4:5], v8 offset0:64 offset1:96
	ds_read2_b32 v[6:7], v8 offset0:128 offset1:160
	ds_read2_b32 v[10:11], v8 offset0:192 offset1:224
	s_mov_b32 s8, 0xf800000
	s_lshr_b32 s2, s30, 3
	s_lshl_b32 s2, s2, 7
	s_add_u32 s2, s2, 0x300000
	s_add_u32 s6, s6, s2
	s_addc_u32 s7, s7, 0
	s_mov_b32 s4, 0
	s_mov_b32 s5, 0x41d00000
	s_mov_b32 s16, 0
	s_mov_b32 s17, 0x420e0000
	s_waitcnt lgkmcnt(0)
	v_min3_f32 v2, v2, v3, v4
	v_min3_f32 v5, v5, v6, v7
	v_min3_f32 v2, v2, v10, v11
	v_min_f32_e32 v2, v2, v5
	s_waitcnt lgkmcnt(0)
	v_add_f32_e32 v20, v20, v21
	v_add_f32_e32 v22, v22, v23
	v_add_f32_e32 v24, v24, v25
	v_add_f32_e32 v26, v26, v27
	v_add_f32_e32 v28, v28, v29
	v_add_f32_e32 v30, v30, v31
	v_add_f32_e32 v32, v32, v33
	v_add_f32_e32 v34, v34, v35
	v_add_f32_e32 v20, v20, v22
	v_add_f32_e32 v24, v24, v26
	v_add_f32_e32 v28, v28, v30
	v_add_f32_e32 v32, v32, v34
	v_add_f32_e32 v20, v20, v24
	v_add_f32_e32 v28, v28, v32
	v_add_f32_e32 v20, v20, v28
	v_add_f32_e32 v2, v2, v20
	v_max_f32_e32 v2, 0, v2
	v_mul_f32_e32 v3, 0x4f800000, v2
	v_cmp_gt_f32_e32 vcc, s8, v2
	s_nop 1
	v_cndmask_b32_e32 v2, v2, v3, vcc
	v_sqrt_f32_e32 v3, v2
	s_nop 0
	v_add_u32_e32 v4, -1, v3
	v_fma_f32 v5, -v4, v3, v2
	v_cmp_ge_f32_e64 s[18:19], 0, v5
	v_add_u32_e32 v5, 1, v3
	s_nop 0
	v_cndmask_b32_e64 v4, v3, v4, s[18:19]
	v_fma_f32 v3, -v5, v3, v2
	v_cmp_lt_f32_e64 s[18:19], 0, v3
	s_nop 1
	v_cndmask_b32_e64 v3, v4, v5, s[18:19]
	v_mul_f32_e32 v4, 0x37800000, v3
	v_cndmask_b32_e32 v3, v3, v4, vcc
	v_mov_b32_e32 v4, 0x260
	v_cmp_class_f32_e32 vcc, v2, v4
	s_nop 1
	v_cndmask_b32_e32 v2, v3, v2, vcc
	s_nop 1
	v_add_f32_dpp v3, v2, v2 quad_perm:[1,0,3,2] row_mask:0xf bank_mask:0xf
	s_nop 1
	v_add_f32_dpp v4, v3, v3 quad_perm:[2,3,0,1] row_mask:0xf bank_mask:0xf
	s_nop 1
	v_add_f32_dpp v5, v4, v4 row_half_mirror row_mask:0xf bank_mask:0xf
	s_nop 1
	v_add_f32_dpp v6, v5, v5 row_mirror row_mask:0xf bank_mask:0xf
	s_nop 1
	v_readlane_b32 s12, v6, 0
	v_readlane_b32 s13, v6, 16
	v_readlane_b32 s14, v6, 32
	v_readlane_b32 s15, v6, 48
	s_nop 3
	v_mov_b32_e32 v7, s12
	v_add_f32_e32 v7, s13, v7
	v_mov_b32_e32 v9, s14
	v_add_f32_e32 v9, s15, v9
	v_add_f32_e32 v0, v7, v9
	v_mov_b32_e32 v4, 0
	s_mov_b64 exec, 1
	v_cvt_f64_f32_e32 v[6:7], v0
	v_add_f64 v[8:9], v[6:7], s[4:5]
	global_atomic_add_f64 v[10:11], v4, v[8:9], s[6:7] sc0
	s_waitcnt vmcnt(0)
	v_cmp_le_f64_e32 vcc, s[16:17], v[10:11]
	s_and_saveexec_b64 s[2:3], vcc
	s_cbranch_execz .Lmain_end
	v_add_f64 v[10:11], v[10:11], -s[16:17]
	v_add_f64 v[10:11], v[10:11], v[6:7]
	v_cvt_f32_f64_e32 v0, v[10:11]
	v_mul_f32_e32 v0, 0x38000000, v0
	global_atomic_add_f32 v4, v0, s[10:11]
